# v26_trimpad
# speedup vs baseline: 1.0026x; 1.0026x over previous
.Lp1_lds_1:
	v_mov_b32_e32 v72, v68
	s_nop 0
	ds_read2_b32 v[66:67], v72 offset1:68
	ds_read2_b32 v[68:69], v72 offset0:136 offset1:204
	s_waitcnt lgkmcnt(0)
	s_branch .Lp1_go_1
	s_nop 0
	s_nop 0
	s_nop 0
	s_nop 0

.Lp1_lds_2:
	v_mov_b32_e32 v8, v4
	s_nop 0
	ds_read2_b32 v[2:3], v8 offset1:68
	ds_read2_b32 v[4:5], v8 offset0:136 offset1:204
	s_waitcnt lgkmcnt(0)
	s_branch .Lp1_go_2
	s_nop 0
	s_nop 0
	s_nop 0
	s_nop 0

.Lp1_lds_4:
	v_mov_b32_e32 v6, v2
	s_nop 0
	ds_read2_b32 v[0:1], v6 offset1:68
	ds_read2_b32 v[2:3], v6 offset0:136 offset1:204
	s_waitcnt lgkmcnt(0)
	s_branch .Lp1_go_4
	s_nop 0
	s_nop 0
	s_nop 0
	s_nop 0
